# speedup vs baseline: 1.0185x; 1.0120x over previous
.Lp_w1t:
	s_sleep 30
	s_load_dwordx2 s[16:17], s[0:1], 0x38
	s_load_dwordx2 s[18:19], s[0:1], 0x40
	s_load_dwordx4 s[20:23], s[0:1], 0x48
	v_lshl_or_b32 v2, s2, 8, v0
	v_add_u32_e32 v2, 0xfffec000, v2
	v_mov_b32_e32 v3, 0
	v_mov_b32_e32 v26, v0
	v_lshrrev_b32_e32 v4, 3, v2
	v_lshrrev_b32_e32 v5, 3, v0
	v_lshlrev_b32_e32 v0, 1, v0
	v_and_b32_e32 v4, 0x1fffffe0, v4
	v_and_b32_e32 v6, 0x80, v0
	v_mov_b32_e32 v7, 0
	v_and_or_b32 v4, v5, 20, v4
	s_waitcnt lgkmcnt(0)
	v_lshl_add_u64 v[8:9], s[8:9], 0, v[6:7]
	v_lshlrev_b32_e32 v6, 2, v1
	v_lshl_add_u64 v[0:1], v[8:9], 0, v[6:7]
	v_or_b32_e32 v6, 1, v4
	v_lshlrev_b64 v[10:11], 8, v[6:7]
	v_or_b32_e32 v6, 2, v4
	v_lshlrev_b64 v[12:13], 8, v[6:7]
	v_or_b32_e32 v6, 3, v4
	v_lshlrev_b64 v[14:15], 8, v[6:7]
	v_or_b32_e32 v6, 8, v4
	v_lshlrev_b64 v[16:17], 8, v[6:7]
	v_or_b32_e32 v6, 9, v4
	v_mov_b32_e32 v5, v7
	v_lshlrev_b64 v[18:19], 8, v[6:7]
	v_or_b32_e32 v6, 10, v4
	v_lshlrev_b64 v[8:9], 8, v[4:5]
	v_lshlrev_b64 v[20:21], 8, v[6:7]
	v_or_b32_e32 v6, 11, v4
	v_lshl_add_u64 v[8:9], v[0:1], 0, v[8:9]
	v_lshlrev_b64 v[4:5], 8, v[6:7]
	v_lshl_add_u64 v[10:11], v[0:1], 0, v[10:11]
	v_lshl_add_u64 v[12:13], v[0:1], 0, v[12:13]
	v_lshl_add_u64 v[14:15], v[0:1], 0, v[14:15]
	v_lshl_add_u64 v[16:17], v[0:1], 0, v[16:17]
	v_lshl_add_u64 v[18:19], v[0:1], 0, v[18:19]
	v_lshl_add_u64 v[20:21], v[0:1], 0, v[20:21]
	v_lshl_add_u64 v[0:1], v[0:1], 0, v[4:5]
	global_load_dword v4, v[8:9], off
	global_load_dword v5, v[10:11], off
	global_load_dword v6, v[12:13], off
	global_load_dword v7, v[14:15], off
	global_load_dword v22, v[16:17], off
	global_load_dword v23, v[18:19], off
	global_load_dword v24, v[20:21], off
	global_load_dword v25, v[0:1], off
	v_lshl_add_u64 v[0:1], v[2:3], 4, s[16:17]
	s_getpc_b64 s[24:25]
	s_and_b32 s24, s24, 0xfffff000
	v_lshlrev_b32_e32 v32, 7, v26
	v_mov_b32_e32 v33, 0
	v_lshl_add_u64 v[34:35], s[24:25], 0, v[32:33]
	global_load_dword v31, v[34:35], off sc0 sc1
	s_waitcnt vmcnt(1)
	v_cvt_pk_f16_f32 v4, v4, v5
	v_cvt_pk_f16_f32 v5, v6, v7
	v_cvt_pk_f16_f32 v6, v22, v23
	v_cvt_pk_f16_f32 v7, v24, v25
	global_store_dwordx4 v[0:1], v[4:7], off sc1
	s_movk_i32 s4, 0x70
	v_cmp_gt_u32_e32 vcc, s4, v26
	s_and_saveexec_b64 s[4:5], vcc
	s_cbranch_execz .Lp_t1
	v_add_co_u32_e32 v34, vcc, 0x8000, v34
	s_nop 1
	v_addc_co_u32_e32 v35, vcc, 0, v35, vcc
	global_load_dword v8, v[34:35], off sc0 sc1
